# baseline (speedup 1.0000x reference)
_Z8k_layer1PKiS0_PKfS2_PK15HIP_vector_typeIjLj4EEPKDv8_DF16_S9_S2_S2_S2_PDF16_PfSB_:
	s_load_dwordx2 s[14:15], s[0:1], 0x48
	s_load_dwordx8 s[4:11], s[0:1], 0x28
	s_load_dwordx2 s[56:57], s[0:1], 0x0
	v_readfirstlane_b32 s13, v0
	s_lshr_b32 s12, s13, 6
	v_and_b32_e32 v178, 63, v0
	v_lshl_or_b32 v2, s12, 10, v178
	v_ashrrev_i32_e32 v3, 31, v2
	v_lshlrev_b64 v[4:5], 4, v[2:3]
	s_lshl_b32 s16, s2, 5
	s_lshl_b32 s17, s12, 3
	s_add_i32 s16, s16, s17
	v_min_i32_e32 v1, 8, v178
	v_add_u32_e32 v1, s16, v1
	v_min_i32_e32 v1, 0xc350, v1
	v_lshlrev_b32_e32 v1, 2, v1
	s_waitcnt lgkmcnt(0)
	global_load_dword v236, v1, s[56:57]
	v_lshl_add_u64 v[6:7], s[6:7], 0, v[4:5]
	s_movk_i32 s3, 0x1000
	v_add_co_u32_e32 v8, vcc, s3, v6
	s_movk_i32 s6, 0x2000
	s_nop 0
	v_addc_co_u32_e32 v9, vcc, 0, v7, vcc
	v_add_co_u32_e32 v10, vcc, s6, v6
	s_movk_i32 s6, 0x3000
	s_nop 0
	v_addc_co_u32_e32 v11, vcc, 0, v7, vcc
	global_load_dwordx4 v[32:35], v[6:7], off
	global_load_dwordx4 v[36:39], v[6:7], off offset:1024
	global_load_dwordx4 v[40:43], v[6:7], off offset:2048
	global_load_dwordx4 v[44:47], v[6:7], off offset:3072
	v_add_co_u32_e32 v6, vcc, s6, v6
	v_lshl_add_u64 v[4:5], s[4:5], 0, v[4:5]
	s_nop 0
	v_addc_co_u32_e32 v7, vcc, 0, v7, vcc
	v_or_b32_e32 v2, 0x200, v2
	global_load_dwordx4 v[48:51], v[8:9], off offset:1024
	global_load_dwordx4 v[52:55], v[8:9], off offset:2048
	global_load_dwordx4 v[56:59], v[10:11], off offset:-4096
	global_load_dwordx4 v[60:63], v[10:11], off
	global_load_dwordx4 v[64:67], v[10:11], off offset:1024
	global_load_dwordx4 v[68:71], v[10:11], off offset:2048
	global_load_dwordx4 v[72:75], v[10:11], off offset:3072
	global_load_dwordx4 v[76:79], v[8:9], off offset:3072
	global_load_dwordx4 v[80:83], v[6:7], off
	global_load_dwordx4 v[84:87], v[6:7], off offset:1024
	global_load_dwordx4 v[88:91], v[6:7], off offset:2048
	global_load_dwordx4 v[92:95], v[6:7], off offset:3072
	v_add_co_u32_e32 v6, vcc, s3, v4
	v_ashrrev_i32_e32 v3, 31, v2
	s_nop 0
	v_addc_co_u32_e32 v7, vcc, 0, v5, vcc
	v_lshl_add_u64 v[2:3], v[2:3], 4, s[4:5]
	global_load_dwordx4 v[96:99], v[4:5], off
	global_load_dwordx4 v[100:103], v[4:5], off offset:1024
	global_load_dwordx4 v[104:107], v[4:5], off offset:2048
	global_load_dwordx4 v[108:111], v[4:5], off offset:3072
	global_load_dwordx4 v[112:115], v[6:7], off
	global_load_dwordx4 v[116:119], v[6:7], off offset:1024
	global_load_dwordx4 v[120:123], v[6:7], off offset:2048
	global_load_dwordx4 v[124:127], v[6:7], off offset:3072
	global_load_dwordx4 v[128:131], v[2:3], off
	global_load_dwordx4 v[132:135], v[2:3], off offset:1024
	global_load_dwordx4 v[136:139], v[2:3], off offset:2048
	global_load_dwordx4 v[140:143], v[2:3], off offset:3072
	v_add_co_u32_e32 v2, vcc, s6, v4
	s_lshl_b32 s3, s12, 4
	s_nop 0
	v_addc_co_u32_e32 v3, vcc, 0, v5, vcc
	global_load_dwordx4 v[144:147], v[2:3], off
	global_load_dwordx4 v[148:151], v[2:3], off offset:1024
	global_load_dwordx4 v[152:155], v[2:3], off offset:2048
	global_load_dwordx4 v[156:159], v[2:3], off offset:3072
	v_and_or_b32 v1, v0, 15, s3
	v_lshlrev_b32_e32 v1, 2, v1
	global_load_dword v179, v1, s[10:11]
	global_load_dword v180, v1, s[14:15]
	v_bfe_u32 v2, v0, 4, 2
	s_lshl_b32 s16, s3, 2
	v_lshl_add_u32 v2, v2, 4, s16
	global_load_dwordx4 v[228:231], v2, s[10:11]
	global_load_dwordx4 v[232:235], v2, s[14:15]
	v_cmp_gt_u32_e32 vcc, 32, v0
	v_lshlrev_b32_e32 v0, 2, v0
	s_and_saveexec_b64 s[4:5], vcc
	v_mov_b32_e32 v1, 0
	v_add_u32_e32 v2, 0xd000, v0
	ds_write2_b32 v2, v1, v1 offset0:176 offset1:208
	s_or_b64 exec, exec, s[4:5]
	global_load_dword v1, v0, s[8:9]
	global_load_dword v2, v0, s[8:9] offset:1024
	s_cmpk_gt_i32 s2, 0x61a
	s_waitcnt vmcnt(0)
	ds_write2st64_b32 v0, v1, v2 offset0:202 offset1:206
	s_waitcnt lgkmcnt(0)
	s_barrier
	s_cbranch_scc1 .LBB3_271
	s_setprio 2
	s_load_dwordx8 s[56:63], s[0:1], 0x0
	s_load_dwordx4 s[4:7], s[0:1], 0x50
	s_mul_i32 s87, s12, 48
	s_lshl_b32 s66, s12, 9
	s_and_b32 s65, s13, 0xffffffc0
	s_lshl_b32 s86, s12, 3
	s_waitcnt lgkmcnt(0)
	v_writelane_b32 v226, s4, 0
	s_add_i32 s87, s87, 0xd200
	s_add_i32 s90, s66, 0xc200
	v_writelane_b32 v226, s5, 1
	v_writelane_b32 v226, s6, 2
	v_writelane_b32 v226, s7, 3
	s_lshl_b32 s4, s12, 12
	s_add_i32 s88, s4, 0x8200
	s_lshl_b32 s5, s12, 1
	s_load_dwordx2 s[72:73], s[0:1], 0x20
	s_load_dwordx2 s[76:77], s[0:1], 0x60
	s_add_u32 s0, s0, 0x68
	s_addc_u32 s1, s1, 0
	v_mbcnt_lo_u32_b32 v0, -1, 0
	v_writelane_b32 v226, s0, 4
	v_mbcnt_hi_u32_b32 v182, -1, v0
	s_mul_i32 s99, s12, 0x2080
	v_writelane_b32 v226, s1, 5
	s_or_b32 s0, s5, 1
	v_and_b32_e32 v0, 64, v182
	s_mov_b32 s91, 0xff800000
	s_lshl_b32 s95, s12, 8
	s_lshl_b32 s64, s0, 8
	s_lshl_b32 s98, s0, 7
	s_add_i32 s93, s4, 0x8500
	s_or_b32 s92, s99, 48
	s_mov_b32 s68, 0
	v_mov_b32_e32 v177, 0
	v_mov_b32_e32 v181, 0xff800000
	s_movk_i32 s69, 0x410
	v_xor_b32_e32 v183, 32, v182
	v_add_u32_e32 v184, 64, v0
	v_xor_b32_e32 v185, 4, v182
	v_xor_b32_e32 v186, 8, v182
	v_xor_b32_e32 v187, 16, v182
	v_mov_b32_e32 v188, 0x3c0
	v_writelane_b32 v226, s92, 6
	s_branch .LBB3_6

.LBB3_127:
	s_setprio 0
	s_mov_b32 s70, s68
	s_mov_b32 s71, s68
	s_mov_b32 s69, s68
	v_mov_b64_e32 v[172:173], s[70:71]
	v_cmp_gt_i32_e32 vcc, 33, v166
	v_lshl_add_u32 v162, v189, 4, s99
	v_mov_b64_e32 v[170:171], s[68:69]
	s_and_b64 vcc, exec, vcc
	ds_write_b128 v162, v[170:173]
	ds_write_b128 v162, v[170:173] offset:2080
	ds_write_b128 v162, v[170:173] offset:4160
	ds_write_b128 v162, v[170:173] offset:6240
	s_cbranch_vccnz .LBB3_129
	v_mov_b64_e32 v[172:173], s[70:71]
	v_mov_b64_e32 v[170:171], s[68:69]
	ds_write_b128 v162, v[170:173] offset:1024
	ds_write_b128 v162, v[170:173] offset:3104
	ds_write_b128 v162, v[170:173] offset:5184
	ds_write_b128 v162, v[170:173] offset:7264

.LBB3_196:
	s_setprio 2
	s_or_b64 exec, exec, s[4:5]
	v_lshlrev_b32_e32 v197, 7, v167
	v_add_u32_e32 v160, s88, v197
	v_lshlrev_b32_e32 v164, 4, v193
	v_add_u32_e32 v198, v160, v164
	s_waitcnt vmcnt(0)
	ds_write_b128 v198, v[20:23]
	ds_write_b128 v198, v[16:19] offset:1024
	ds_write_b128 v198, v[28:31] offset:2048
	ds_write_b128 v198, v[24:27] offset:3072
	s_add_i32 s0, s78, s33
	s_add_i32 s0, s0, s96
	v_add_u32_e32 v160, s0, v194
	v_min_i32_e32 v168, s79, v160
	v_add_u32_e32 v169, 8, v160
	v_add_u32_e32 v170, 16, v160
	v_add_u32_e32 v171, 24, v160
	v_min_i32_e32 v169, s79, v169
	v_min_i32_e32 v170, s79, v170
	v_min_i32_e32 v171, s79, v171
	v_lshl_add_u32 v168, v168, 2, s90
	v_lshl_add_u32 v169, v169, 2, s90
	v_lshl_add_u32 v170, v170, 2, s90
	v_lshl_add_u32 v171, v171, 2, s90
	ds_read_b32 v168, v168
	ds_read_b32 v169, v169
	ds_read_b32 v170, v170
	ds_read_b32 v171, v171
	s_waitcnt lgkmcnt(3)
	v_lshl_or_b32 v176, v168, 3, v193
	v_lshl_add_u64 v[16:17], v[176:177], 4, s[72:73]
	global_load_dwordx4 v[16:19], v[16:17], off
	s_waitcnt lgkmcnt(2)
	v_lshl_or_b32 v176, v169, 3, v193
	v_lshl_add_u64 v[24:25], v[176:177], 4, s[72:73]
	global_load_dwordx4 v[24:27], v[24:25], off
	s_waitcnt lgkmcnt(1)
	v_lshl_or_b32 v176, v170, 3, v193
	v_lshl_add_u64 v[20:21], v[176:177], 4, s[72:73]
	global_load_dwordx4 v[20:23], v[20:21], off
	s_waitcnt lgkmcnt(0)
	v_lshl_or_b32 v176, v171, 3, v193
	v_lshl_add_u64 v[28:29], v[176:177], 4, s[72:73]
	global_load_dwordx4 v[28:31], v[28:29], off
